# SGU LayerNorm row sums: xor 1/2/4/8 via DPP adds and xor 16 via v_permlane16_swap instead of 20 ds_bpermute round trips per iteration (bit-identical), on top of the attention changes
# speedup vs baseline: 1.0065x; 1.0065x over previous
; #define GAS __attribute__((address_space(1)))
; __device__ __forceinline__ void phase_sgu(const Frame& F, const Args& a) {
;     ...
;           for (int pass = 0; pass < 8; ++pass) { const int q = pass * 16 + rg;
;             const u32x4 raw = *(const GAS u32x4*)(Z + (size_t)(r0 + q) * 3072 + 2048 + cb);
;             float x[8] = {bflo(raw.x), bfhi(raw.x), bflo(raw.y), bfhi(raw.y), bflo(raw.z), bfhi(raw.z), bflo(raw.w), bfhi(raw.w)};
;             float s = 0.f;
; #pragma unroll
;             for (int i = 0; i < 8; ++i) s += x[i];
; #pragma unroll
;             for (int o = 1; o < 32; o <<= 1) s += __shfl_xor(s, o);
;             const float mean = s * (1.0f / 256.0f); float ss = 0.f;
; #pragma unroll
;             for (int i = 0; i < 8; ++i) { x[i] -= mean; ss += x[i] * x[i]; }
; #pragma unroll
;             for (int o = 1; o < 32; o <<= 1) ss += __shfl_xor(ss, o);
;             const float rstd = rsqrtf(ss * (1.0f / 256.0f) + LN_EPS);
.LBB0_590:
	v_add_u32_e32 v29, s22, v23
	v_mov_b64_e32 v[24:25], s[6:7]
	v_mad_i64_i32 v[26:27], s[0:1], v29, s17, v[24:25]
	v_add_u32_e32 v28, s22, v158
	v_add_u32_e32 v29, 16, v29
	v_lshl_add_u64 v[26:27], v[26:27], 0, v[124:125]
	v_xor_b32_e32 v30, v28, v122
	v_add_u32_e32 v28, 16, v28
	v_mad_i64_i32 v[24:25], s[0:1], v29, s17, v[24:25]
	v_add_co_u32_e32 v26, vcc, 0x1000, v26
	v_xor_b32_e32 v28, v28, v122
	v_lshl_add_u64 v[24:25], v[24:25], 0, v[124:125]
	v_addc_co_u32_e32 v27, vcc, 0, v27, vcc
	v_lshl_add_u32 v49, v28, 1, v168
	v_add_co_u32_e32 v28, vcc, s14, v24
	v_lshl_add_u32 v48, v30, 1, v168
	s_nop 0
	v_addc_co_u32_e32 v29, vcc, 0, v25, vcc
	global_load_dwordx4 v[24:27], v[26:27], off
	s_nop 0
	global_load_dwordx4 v[28:31], v[28:29], off
	s_add_i32 s22, s22, 32
	s_cmpk_eq_i32 s22, 0x80
	s_waitcnt vmcnt(1)
	v_lshlrev_b32_e32 v50, 16, v24
	v_and_b32_e32 v51, 0xffff0000, v24
	s_waitcnt vmcnt(0)
	v_lshlrev_b32_e32 v52, 16, v28
	v_and_b32_e32 v36, 0xffff0000, v30
	v_lshlrev_b32_e32 v37, 16, v30
	v_add_f32_e32 v30, 0, v50
	v_and_b32_e32 v32, 0xffff0000, v27
	v_lshlrev_b32_e32 v33, 16, v27
	v_and_b32_e32 v34, 0xffff0000, v26
	v_lshlrev_b32_e32 v35, 16, v26
	v_and_b32_e32 v24, 0xffff0000, v25
	v_lshlrev_b32_e32 v25, 16, v25
	v_and_b32_e32 v53, 0xffff0000, v28
	v_and_b32_e32 v26, 0xffff0000, v31
	v_lshlrev_b32_e32 v27, 16, v31
	v_add_f32_e32 v31, 0, v52
	v_add_f32_e32 v30, v30, v51
	v_and_b32_e32 v28, 0xffff0000, v29
	v_lshlrev_b32_e32 v29, 16, v29
	v_add_f32_e32 v31, v31, v53
	v_add_f32_e32 v30, v30, v25
	v_add_f32_e32 v31, v31, v29
	v_add_f32_e32 v30, v30, v24
	v_add_f32_e32 v31, v31, v28
	v_add_f32_e32 v30, v30, v35
	v_add_f32_e32 v31, v31, v37
	v_add_f32_e32 v30, v30, v34
	v_add_f32_e32 v31, v31, v36
	v_add_f32_e32 v30, v30, v33
	v_add_f32_e32 v31, v31, v27
	v_add_f32_e32 v30, v30, v32
	v_add_f32_e32 v31, v31, v26
	s_nop 1
	v_add_f32_dpp v30, v30, v30 quad_perm:[1,0,3,2] row_mask:0xf bank_mask:0xf
	v_add_f32_dpp v31, v31, v31 quad_perm:[1,0,3,2] row_mask:0xf bank_mask:0xf
	s_nop 0
	v_add_f32_dpp v30, v30, v30 quad_perm:[2,3,0,1] row_mask:0xf bank_mask:0xf
	v_add_f32_dpp v31, v31, v31 quad_perm:[2,3,0,1] row_mask:0xf bank_mask:0xf
	s_nop 0
	v_add_f32_dpp v30, v30, v30 row_half_mirror row_mask:0xf bank_mask:0xf
	v_add_f32_dpp v31, v31, v31 row_half_mirror row_mask:0xf bank_mask:0xf
	s_nop 0
	v_add_f32_dpp v30, v30, v30 row_mirror row_mask:0xf bank_mask:0xf
	v_add_f32_dpp v31, v31, v31 row_mirror row_mask:0xf bank_mask:0xf
	v_mov_b32_e32 v38, v30
	v_mov_b32_e32 v39, v31
	s_nop 1
	v_permlane16_swap_b32 v38, v30
	v_permlane16_swap_b32 v39, v31
	v_add_f32_e32 v38, v30, v38
	v_add_f32_e32 v31, v31, v39
	v_mul_f32_e32 v30, 0x3b800000, v38
	v_fmac_f32_e32 v51, 0xbb800000, v38
	v_fmac_f32_e32 v50, 0xbb800000, v38
	v_mul_f32_e32 v38, 0x3b800000, v31
	v_fmac_f32_e32 v53, 0xbb800000, v31
	v_mul_f32_e32 v54, v51, v51
	v_pk_add_f32 v[24:25], v[24:25], v[30:31] op_sel_hi:[1,0] neg_lo:[0,1] neg_hi:[0,1]
	v_fmac_f32_e32 v52, 0xbb800000, v31
	v_pk_add_f32 v[34:35], v[34:35], v[30:31] op_sel_hi:[1,0] neg_lo:[0,1] neg_hi:[0,1]
	v_pk_add_f32 v[30:31], v[32:33], v[30:31] op_sel_hi:[1,0] neg_lo:[0,1] neg_hi:[0,1]
	v_mul_f32_e32 v55, v53, v53
	v_pk_add_f32 v[28:29], v[28:29], v[38:39] op_sel_hi:[1,0] neg_lo:[0,1] neg_hi:[0,1]
	v_pk_add_f32 v[32:33], v[36:37], v[38:39] op_sel_hi:[1,0] neg_lo:[0,1] neg_hi:[0,1]
	v_fmac_f32_e32 v54, v50, v50
	v_pk_mul_f32 v[36:37], v[24:25], v[24:25]
	v_fmac_f32_e32 v55, v52, v52
	v_pk_mul_f32 v[42:43], v[28:29], v[28:29]
	v_add_f32_e32 v37, v37, v54
	v_pk_add_f32 v[26:27], v[26:27], v[38:39] op_sel_hi:[1,0] neg_lo:[0,1] neg_hi:[0,1]
	v_pk_mul_f32 v[38:39], v[34:35], v[34:35]
	v_add_f32_e32 v43, v43, v55
	v_add_f32_e32 v36, v36, v37
	v_pk_mul_f32 v[44:45], v[32:33], v[32:33]
	v_add_f32_e32 v37, v42, v43
	v_add_f32_e32 v36, v39, v36
	v_pk_mul_f32 v[40:41], v[30:31], v[30:31]
	v_add_f32_e32 v37, v45, v37
	v_add_f32_e32 v36, v38, v36
	v_pk_mul_f32 v[46:47], v[26:27], v[26:27]
	v_add_f32_e32 v37, v44, v37
	v_add_f32_e32 v36, v41, v36
	v_add_f32_e32 v37, v47, v37
	v_add_f32_e32 v36, v40, v36
	v_add_f32_e32 v37, v46, v37
	s_nop 1
	v_add_f32_dpp v36, v36, v36 quad_perm:[1,0,3,2] row_mask:0xf bank_mask:0xf
	v_add_f32_dpp v37, v37, v37 quad_perm:[1,0,3,2] row_mask:0xf bank_mask:0xf
	s_nop 0
	v_add_f32_dpp v36, v36, v36 quad_perm:[2,3,0,1] row_mask:0xf bank_mask:0xf
	v_add_f32_dpp v37, v37, v37 quad_perm:[2,3,0,1] row_mask:0xf bank_mask:0xf
	s_nop 0
	v_add_f32_dpp v36, v36, v36 row_half_mirror row_mask:0xf bank_mask:0xf
	v_add_f32_dpp v37, v37, v37 row_half_mirror row_mask:0xf bank_mask:0xf
	s_nop 0
	v_add_f32_dpp v36, v36, v36 row_mirror row_mask:0xf bank_mask:0xf
	v_add_f32_dpp v37, v37, v37 row_mirror row_mask:0xf bank_mask:0xf
	v_mov_b32_e32 v38, v36
	v_mov_b32_e32 v39, v37
	s_nop 1
	v_permlane16_swap_b32 v38, v36
	v_permlane16_swap_b32 v39, v37
	v_add_f32_e32 v36, v36, v38
	v_add_f32_e32 v37, v37, v39
	v_fmamk_f32 v36, v36, 0x3b800000, v190
	v_fmamk_f32 v37, v37, 0x3b800000, v190
	v_mul_f32_e32 v38, 0x4b800000, v36
	v_cmp_gt_f32_e64 s[0:1], s18, v36
	v_mul_f32_e32 v39, 0x4b800000, v37
	v_cmp_gt_f32_e32 vcc, s18, v37
	v_cndmask_b32_e64 v36, v36, v38, s[0:1]
	v_rsq_f32_e32 v36, v36
	v_cndmask_b32_e32 v37, v37, v39, vcc
	v_rsq_f32_e32 v37, v37
	v_mul_f32_e32 v38, 0x45800000, v36
	v_cndmask_b32_e64 v36, v36, v38, s[0:1]
	v_mul_f32_e32 v39, 0x45800000, v37
	v_cndmask_b32_e32 v37, v37, v39, vcc
	v_mul_f32_e32 v38, v50, v36
	v_mul_f32_e32 v39, v51, v36
	v_mul_f32_e32 v25, v25, v36
	v_mul_f32_e32 v24, v24, v36
	v_mul_f32_e32 v35, v35, v36
	v_mul_f32_e32 v34, v34, v36
	v_mul_f32_e32 v31, v31, v36
	v_mul_f32_e32 v30, v30, v36
; #define LAS __attribute__((address_space(3)))
; __device__ __forceinline__ unsigned f2bf(float f) { unsigned u = __builtin_bit_cast(unsigned, f); return (u + 0x7fffu + ((u >> 16) & 1u)) >> 16; }
; __device__ __forceinline__ void phase_sgu(const Frame& F, const Args& a) {
;     ...
; #pragma unroll
;             for (int i = 0; i < 8; ++i) { const float gg = i < 4 ? lg0[i & 3] : lg1[i & 3], bb = i < 4 ? lb0[i & 3] : lb1[i & 3];
;                 vT[(8 * c8 + i) * 136 + (q ^ ((c8 & 15) << 3))] = (bf16_t)f2bf(x[i] * rstd * gg + bb); } } }
;         __syncthreads();
;         const int pm = F.wave & 1, cn = F.wave >> 1;
;         f32x4 acc[4][4];
; #pragma unroll
;         for (int m = 0; m < 4; ++m)
; #pragma unroll
;             for (int n = 0; n < 4; ++n) acc[m][n] = (f32x4){0.f, 0.f, 0.f, 0.f};
; #pragma unroll
;         for (int kk = 0; kk < 4; ++kk) { bf16x8 am[4], bn[4];
; #pragma unroll
;             for (int m = 0; m < 4; ++m) am[m] = *(const LAS bf16x8*)(wA + (64 * pm + 16 * m + fr) * 136 + 32 * kk + 8 * fq);
; #pragma unroll
;             for (int n = 0; n < 4; ++n) { const int cr = 64 * cn + 16 * n + fr; bn[n] = *(const LAS bf16x8*)(vT + cr * 136 + ((32 * kk + 8 * fq) ^ (((cr >> 3) & 15) << 3))); }
; #pragma unroll
;             for (int m = 0; m < 4; ++m)
; #pragma unroll
;                 for (int n = 0; n < 4; ++n) acc[m][n] = __builtin_amdgcn_mfma_f32_16x16x32_bf16(bn[n], am[m], acc[m][n], 0, 0, 0); }
	v_mul_f32_e32 v36, v52, v37
	v_mul_f32_e32 v40, v53, v37
	v_mul_f32_e32 v29, v29, v37
	v_mul_f32_e32 v28, v28, v37
	v_mul_f32_e32 v33, v33, v37
	v_mul_f32_e32 v32, v32, v37
	v_mul_f32_e32 v27, v27, v37
	v_mul_f32_e32 v26, v26, v37
	v_fma_f32 v37, v10, v38, v14
	v_fma_f32 v38, v11, v39, v15
	v_fma_f32 v25, v12, v25, v16
	v_fma_f32 v24, v13, v24, v17
	v_fma_f32 v35, v2, v35, v6
	v_fma_f32 v34, v3, v34, v7
	v_fma_f32 v31, v4, v31, v8
	v_fma_f32 v30, v5, v30, v9
	v_fma_f32 v36, v10, v36, v14
	v_fma_f32 v39, v11, v40, v15
	v_fma_f32 v29, v12, v29, v16
	v_fma_f32 v28, v13, v28, v17
	v_fma_f32 v33, v2, v33, v6
	v_fma_f32 v32, v3, v32, v7
	v_fma_f32 v27, v4, v27, v8
	v_fma_f32 v26, v5, v26, v9
	v_bfe_u32 v40, v37, 16, 1
	v_bfe_u32 v41, v38, 16, 1
	v_bfe_u32 v42, v25, 16, 1
	v_bfe_u32 v43, v24, 16, 1
	v_bfe_u32 v44, v35, 16, 1
	v_bfe_u32 v45, v34, 16, 1
	v_bfe_u32 v46, v31, 16, 1
	v_bfe_u32 v47, v30, 16, 1
	v_bfe_u32 v50, v36, 16, 1
	v_bfe_u32 v51, v39, 16, 1
	v_bfe_u32 v52, v29, 16, 1
	v_bfe_u32 v53, v28, 16, 1
	v_bfe_u32 v54, v33, 16, 1
	v_bfe_u32 v55, v32, 16, 1
	v_bfe_u32 v56, v27, 16, 1
	v_bfe_u32 v57, v26, 16, 1
	v_add3_u32 v37, v37, v40, s15
	v_add3_u32 v38, v38, v41, s15
	v_add3_u32 v25, v25, v42, s15
	v_add3_u32 v24, v24, v43, s15
	v_add3_u32 v35, v35, v44, s15
	v_add3_u32 v34, v34, v45, s15
	v_add3_u32 v31, v31, v46, s15
	v_add3_u32 v30, v30, v47, s15
	v_add3_u32 v36, v36, v50, s15
	v_add3_u32 v39, v39, v51, s15
	v_add3_u32 v29, v29, v52, s15
	v_add3_u32 v28, v28, v53, s15
	v_add3_u32 v33, v33, v54, s15
	v_add3_u32 v32, v32, v55, s15
	v_add3_u32 v27, v27, v56, s15
	v_add3_u32 v26, v26, v57, s15
	ds_write_b16_d16_hi v48, v37 offset:34816
	ds_write_b16_d16_hi v48, v38 offset:35088
	ds_write_b16_d16_hi v48, v25 offset:35360
	ds_write_b16_d16_hi v48, v24 offset:35632
	ds_write_b16_d16_hi v48, v35 offset:35904
	ds_write_b16_d16_hi v48, v34 offset:36176
	ds_write_b16_d16_hi v48, v31 offset:36448
	ds_write_b16_d16_hi v48, v30 offset:36720
	ds_write_b16_d16_hi v49, v36 offset:34816
	ds_write_b16_d16_hi v49, v39 offset:35088
	ds_write_b16_d16_hi v49, v29 offset:35360
	ds_write_b16_d16_hi v49, v28 offset:35632
	ds_write_b16_d16_hi v49, v33 offset:35904
	ds_write_b16_d16_hi v49, v32 offset:36176
	ds_write_b16_d16_hi v49, v27 offset:36448
	ds_write_b16_d16_hi v49, v26 offset:36720
	s_cbranch_scc0 .LBB0_590
	s_waitcnt lgkmcnt(0)
	s_barrier
	ds_read_b128 v[6:9], v173 offset:34816
	ds_read_b128 v[10:13], v174 offset:34816
	ds_read_b128 v[2:5], v191
	ds_read_b128 v[86:89], v191 offset:64
	ds_read_b128 v[14:17], v175 offset:34816
	ds_read_b128 v[26:29], v176 offset:34816
	s_waitcnt lgkmcnt(3)
	v_mfma_f32_16x16x32_bf16 v[18:21], v[6:9], v[2:5], 0
	v_add_u32_e32 v144, s21, v189
	v_ashrrev_i32_e32 v145, 31, v144
	v_or_b32_e32 v154, s2, v169
	v_mfma_f32_16x16x32_bf16 v[114:117], v[10:13], v[2:5], 0
	v_mov_b64_e32 v[148:149], s[6:7]
	v_lshlrev_b32_e32 v38, 2, v169
	v_readlane_b32 s36, v254, 5
	s_waitcnt lgkmcnt(1)
	v_mfma_f32_16x16x32_bf16 v[102:105], v[14:17], v[2:5], 0
	v_lshlrev_b64 v[146:147], 1, v[144:145]
	v_lshl_or_b32 v124, s20, 9, v38
	v_readlane_b32 s48, v254, 17
	s_waitcnt lgkmcnt(0)
	v_mfma_f32_16x16x32_bf16 v[94:97], v[26:29], v[2:5], 0
	ds_read_b128 v[2:5], v191 offset:4352
	ds_read_b128 v[74:77], v191 offset:4416
	ds_read_b128 v[22:25], v191 offset:8704
	ds_read_b128 v[30:33], v191 offset:8768
	v_readlane_b32 s49, v254, 18
	s_waitcnt lgkmcnt(3)
	v_mfma_f32_16x16x32_bf16 v[98:101], v[6:9], v[2:5], 0
	v_mov_b32_e32 v129, v125
	v_ashrrev_i32_e32 v155, 31, v154
	s_add_i32 s12, s12, 1
	v_mfma_f32_16x16x32_bf16 v[90:93], v[10:13], v[2:5], 0
	v_readlane_b32 s37, v254, 6
	v_readlane_b32 s38, v254, 7
	v_readlane_b32 s39, v254, 8
	v_mfma_f32_16x16x32_bf16 v[82:85], v[14:17], v[2:5], 0
	v_readlane_b32 s40, v254, 9
	v_readlane_b32 s41, v254, 10
	v_readlane_b32 s42, v254, 11
	v_mfma_f32_16x16x32_bf16 v[78:81], v[26:29], v[2:5], 0
	ds_read_b128 v[34:37], v191 offset:13056
	ds_read_b128 v[2:5], v191 offset:13120
	global_load_dword v127, v124, s[48:49]
	v_readlane_b32 s43, v254, 12
	s_waitcnt lgkmcnt(3)
	v_mfma_f32_16x16x32_bf16 v[66:69], v[6:9], v[22:25], 0
	v_readlane_b32 s44, v254, 13
	v_readlane_b32 s45, v254, 14
	v_readlane_b32 s46, v254, 15
	s_waitcnt lgkmcnt(1)
	v_mfma_f32_16x16x32_bf16 v[54:57], v[6:9], v[34:37], 0
	v_mad_i64_i32 v[6:7], s[0:1], v154, s17, v[148:149]
	v_lshl_add_u64 v[150:151], v[6:7], 0, v[146:147]
	global_load_dwordx2 v[152:153], v[150:151], off offset:2048
	ds_read_b128 v[70:73], v177 offset:34816
	ds_read_b128 v[46:49], v178 offset:34816
	v_mfma_f32_16x16x32_bf16 v[62:65], v[10:13], v[22:25], 0
	v_lshlrev_b64 v[154:155], 11, v[154:155]
	v_lshl_add_u64 v[154:155], s[92:93], 0, v[154:155]
	v_lshl_add_u64 v[198:199], v[154:155], 0, s[10:11]
	v_mfma_f32_16x16x32_bf16 v[58:61], v[14:17], v[22:25], 0
	v_readlane_b32 s47, v254, 16
	v_readlane_b32 s50, v254, 19
	v_readlane_b32 s51, v254, 20
	v_mfma_f32_16x16x32_bf16 v[50:53], v[26:29], v[22:25], 0
	v_mfma_f32_16x16x32_bf16 v[42:45], v[10:13], v[34:37], 0
	v_mfma_f32_16x16x32_bf16 v[22:25], v[14:17], v[34:37], 0
	v_mfma_f32_16x16x32_bf16 v[26:29], v[26:29], v[34:37], 0
	ds_read_b128 v[38:41], v179 offset:34816
	ds_read_b128 v[34:37], v180 offset:34816
	ds_read_b128 v[14:17], v181 offset:34816
	ds_read_b128 v[10:13], v182 offset:34816
	s_waitcnt lgkmcnt(5)
	v_mfma_f32_16x16x32_bf16 v[118:121], v[70:73], v[86:89], v[18:21]
	ds_read_b128 v[110:113], v191 offset:128
	ds_read_b128 v[106:109], v191 offset:192
	s_nop 0
	ds_read_b128 v[18:21], v185 offset:34816
	ds_read_b128 v[6:9], v186 offset:34816
	global_load_dword v131, v124, s[48:49] offset:64
	global_load_dword v133, v124, s[48:49] offset:128
	s_nop 0
	global_load_dword v124, v124, s[48:49] offset:192
	s_waitcnt lgkmcnt(3)
; #define GAS __attribute__((address_space(1)))
; #define LAS __attribute__((address_space(3)))
; __device__ __forceinline__ unsigned pk4_fp8(float a, float b, float c, float d) { int w = 0; w = __builtin_amdgcn_cvt_pk_fp8_f32(sat8(a), sat8(b), w, false); w = __builtin_amdgcn_cvt_pk_fp8_f32(sat8(c), sat8(d), w, true); return (unsigned)w; }
; __device__ __forceinline__ void phase_sgu(const Frame& F, const Args& a) {
;     ...
;         for (int kk = 0; kk < 4; ++kk) { bf16x8 am[4], bn[4];
; #pragma unroll
;             for (int m = 0; m < 4; ++m) am[m] = *(const LAS bf16x8*)(wA + (64 * pm + 16 * m + fr) * 136 + 32 * kk + 8 * fq);
; #pragma unroll
;             for (int n = 0; n < 4; ++n) { const int cr = 64 * cn + 16 * n + fr; bn[n] = *(const LAS bf16x8*)(vT + cr * 136 + ((32 * kk + 8 * fq) ^ (((cr >> 3) & 15) << 3))); }
; #pragma unroll
;             for (int m = 0; m < 4; ++m)
; #pragma unroll
;                 for (int n = 0; n < 4; ++n) acc[m][n] = __builtin_amdgcn_mfma_f32_16x16x32_bf16(bn[n], am[m], acc[m][n], 0, 0, 0); }
; #pragma unroll
;         for (int m = 0; m < 4; ++m) { const int p = 64 * pm + 16 * m + fr, row = r0 + p; const float bias = a.in[I_SBS][g * 128 + p];
; #pragma unroll
;             for (int n = 0; n < 4; ++n) { const int c = g * 256 + 64 * cn + 16 * n + 4 * fq;
;                 const u32x2 uu = *(const GAS u32x2*)(Z + (size_t)row * 3072 + 1024 + c);
;                 const float s0 = bflo(uu.x) * (acc[m][n][0] + bias), s1 = bfhi(uu.x) * (acc[m][n][1] + bias), s2 = bflo(uu.y) * (acc[m][n][2] + bias), s3 = bfhi(uu.y) * (acc[m][n][3] + bias);
;                 *(GAS unsigned*)((unsigned char*)MIX + (size_t)row * D + 1024 + c) = pk4_fp8(s0, s1, s2, s3); } }
	v_mfma_f32_16x16x32_bf16 v[118:121], v[14:17], v[110:113], v[118:121]
	s_waitcnt lgkmcnt(1)
	v_mfma_f32_16x16x32_bf16 v[118:121], v[18:21], v[106:109], v[118:121]
	v_mfma_f32_16x16x32_bf16 v[194:197], v[38:41], v[86:89], v[102:105]
	v_mfma_f32_16x16x32_bf16 v[114:117], v[46:49], v[86:89], v[114:117]
	s_waitcnt vmcnt(4)
	s_nop 4
	v_add_f32_e32 v118, v118, v127
	v_add_f32_e32 v119, v119, v127
	v_add_f32_e32 v120, v120, v127
	v_add_f32_e32 v102, v121, v127
	v_mfma_f32_16x16x32_bf16 v[114:117], v[10:13], v[110:113], v[114:117]
	s_waitcnt vmcnt(3)
	v_lshlrev_b32_e32 v103, 16, v152
	v_and_b32_e32 v104, 0xffff0000, v152
	v_mul_f32_e32 v103, v118, v103
	v_mul_f32_e32 v104, v119, v104
	v_med3_f32 v103, v103, s19, v193
	v_med3_f32 v104, v104, s19, v193
	v_cvt_pk_fp8_f32 v129, v103, v104
	v_lshlrev_b32_e32 v105, 16, v153
	v_and_b32_e32 v121, 0xffff0000, v153
	v_mul_f32_e32 v105, v120, v105
	v_mul_f32_e32 v102, v102, v121
	v_med3_f32 v103, v105, s19, v193
	v_med3_f32 v102, v102, s19, v193
	v_cvt_pk_fp8_f32 v129, v103, v102 op_sel:[0,0,1]
	v_lshl_add_u64 v[102:103], v[198:199], 0, v[144:145]
	s_waitcnt lgkmcnt(0)
	v_mfma_f32_16x16x32_bf16 v[114:117], v[6:9], v[106:109], v[114:117]
	v_mov_b32_e32 v118, v125
	global_store_dword v[102:103], v129, off
	global_load_dwordx2 v[102:103], v[150:151], off offset:2080
	v_or_b32_e32 v104, 16, v144
	v_mfma_f32_16x16x32_bf16 v[152:155], v[46:49], v[74:77], v[90:93]
	s_nop 2
	v_add_f32_e32 v105, v114, v127
	v_add_f32_e32 v114, v115, v127
	v_add_f32_e32 v115, v116, v127
	v_add_f32_e32 v116, v117, v127
	v_mov_b32_e32 v129, v125
	v_mfma_f32_16x16x32_bf16 v[82:85], v[38:41], v[74:77], v[82:85]
	s_waitcnt vmcnt(0)
	v_lshlrev_b32_e32 v117, 16, v102
	v_and_b32_e32 v102, 0xffff0000, v102
	v_mul_f32_e32 v105, v105, v117
	v_mul_f32_e32 v102, v114, v102
	v_med3_f32 v105, v105, s19, v193
	v_med3_f32 v102, v102, s19, v193
	v_cvt_pk_fp8_f32 v118, v105, v102
	v_lshlrev_b32_e32 v119, 16, v103
	v_and_b32_e32 v103, 0xffff0000, v103
	v_mul_f32_e32 v114, v115, v119
	v_mul_f32_e32 v102, v116, v103
	v_med3_f32 v103, v114, s19, v193
	v_med3_f32 v102, v102, s19, v193
	v_cvt_pk_fp8_f32 v118, v103, v102 op_sel:[0,0,1]
	v_ashrrev_i32_e32 v105, 31, v104
	v_lshl_add_u64 v[102:103], v[198:199], 0, v[104:105]
	v_mfma_f32_16x16x32_bf16 v[114:117], v[34:37], v[86:89], v[94:97]
	global_store_dword v[102:103], v118, off
	global_load_dwordx2 v[200:201], v[150:151], off offset:2112
	v_or_b32_e32 v102, 32, v144
	v_mfma_f32_16x16x32_bf16 v[118:121], v[70:73], v[74:77], v[98:101]
	s_waitcnt vmcnt(0)
	v_lshlrev_b32_e32 v141, 16, v200
	s_nop 0
	ds_read_b128 v[98:101], v183 offset:34816
	ds_read_b128 v[94:97], v187 offset:34816
	ds_read_b128 v[90:93], v184 offset:34816
	s_waitcnt lgkmcnt(2)
	v_mfma_f32_16x16x32_bf16 v[194:197], v[98:101], v[110:113], v[194:197]
	v_and_b32_e32 v143, 0xffff0000, v200
	ds_read_b128 v[86:89], v188 offset:34816
	s_waitcnt lgkmcnt(2)
	v_mfma_f32_16x16x32_bf16 v[194:197], v[94:97], v[106:109], v[194:197]
	s_waitcnt lgkmcnt(1)
	v_mfma_f32_16x16x32_bf16 v[110:113], v[90:93], v[110:113], v[114:117]
	s_waitcnt lgkmcnt(0)
	v_mfma_f32_16x16x32_bf16 v[106:109], v[86:89], v[106:109], v[110:113]
	s_nop 3
	v_add_f32_e32 v103, v194, v127
	v_add_f32_e32 v135, v195, v127
	v_mul_f32_e32 v103, v103, v141
	v_mul_f32_e32 v135, v135, v143
	v_med3_f32 v103, v103, s19, v193
	v_med3_f32 v135, v135, s19, v193
	v_cvt_pk_fp8_f32 v129, v103, v135
	v_add_f32_e32 v137, v196, v127
	v_add_f32_e32 v139, v197, v127
	v_lshlrev_b32_e32 v194, 16, v201
	v_and_b32_e32 v195, 0xffff0000, v201
	v_mul_f32_e32 v137, v137, v194
	v_mul_f32_e32 v103, v139, v195
	v_med3_f32 v135, v137, s19, v193
	v_med3_f32 v103, v103, s19, v193
	v_cvt_pk_fp8_f32 v129, v135, v103 op_sel:[0,0,1]
	v_ashrrev_i32_e32 v103, 31, v102
	v_lshl_add_u64 v[194:195], v[198:199], 0, v[102:103]
	v_add_f32_e32 v106, v106, v127
	global_store_dword v[194:195], v129, off
	global_load_dwordx2 v[150:151], v[150:151], off offset:2144
	v_add_f32_e32 v107, v107, v127
	v_mfma_f32_16x16x32_bf16 v[76:79], v[34:37], v[74:77], v[78:81]
	v_add_f32_e32 v108, v108, v127
	v_add_f32_e32 v109, v109, v127
	v_or_b32_e32 v74, 48, v144
	v_mov_b32_e32 v81, v125
	v_or_b32_e32 v80, s2, v170
	v_ashrrev_i32_e32 v75, 31, v74
	v_mad_i64_i32 v[114:115], s[0:1], v80, s17, v[148:149]
	v_mov_b32_e32 v127, v125
	v_mfma_f32_16x16x32_bf16 v[66:69], v[70:73], v[30:33], v[66:69]
	s_waitcnt vmcnt(0)
	v_lshlrev_b32_e32 v110, 16, v150
	v_and_b32_e32 v111, 0xffff0000, v150
	v_mul_f32_e32 v106, v106, v110
	v_mul_f32_e32 v107, v107, v111
	v_med3_f32 v106, v106, s19, v193
	v_med3_f32 v107, v107, s19, v193
	v_cvt_pk_fp8_f32 v81, v106, v107
	v_lshlrev_b32_e32 v112, 16, v151
	v_and_b32_e32 v113, 0xffff0000, v151
	v_mul_f32_e32 v108, v108, v112
	v_mul_f32_e32 v106, v109, v113
	v_med3_f32 v107, v108, s19, v193
	v_med3_f32 v106, v106, s19, v193
	v_cvt_pk_fp8_f32 v81, v107, v106 op_sel:[0,0,1]
	v_lshl_add_u64 v[106:107], v[198:199], 0, v[74:75]
	v_lshl_add_u64 v[150:151], v[114:115], 0, v[146:147]
	v_mfma_f32_16x16x32_bf16 v[62:65], v[46:49], v[30:33], v[62:65]
	global_store_dword v[106:107], v81, off
	global_load_dwordx2 v[194:195], v[150:151], off offset:2048
	ds_read_b128 v[106:109], v191 offset:4480
	ds_read_b128 v[110:113], v191 offset:4544
	s_waitcnt lgkmcnt(1)
	v_mfma_f32_16x16x32_bf16 v[114:117], v[14:17], v[106:109], v[118:121]
	v_ashrrev_i32_e32 v81, 31, v80
	v_lshlrev_b64 v[80:81], 11, v[80:81]
	v_lshl_add_u64 v[80:81], s[92:93], 0, v[80:81]
	s_waitcnt lgkmcnt(0)
	v_mfma_f32_16x16x32_bf16 v[114:117], v[18:21], v[110:113], v[114:117]
	s_waitcnt vmcnt(0)
; #define GAS __attribute__((address_space(1)))
; #define LAS __attribute__((address_space(3)))
; __device__ __forceinline__ unsigned pk4_fp8(float a, float b, float c, float d) { int w = 0; w = __builtin_amdgcn_cvt_pk_fp8_f32(sat8(a), sat8(b), w, false); w = __builtin_amdgcn_cvt_pk_fp8_f32(sat8(c), sat8(d), w, true); return (unsigned)w; }
; __device__ __forceinline__ void phase_sgu(const Frame& F, const Args& a) {
;     ...
;         for (int kk = 0; kk < 4; ++kk) { bf16x8 am[4], bn[4];
; #pragma unroll
;             for (int m = 0; m < 4; ++m) am[m] = *(const LAS bf16x8*)(wA + (64 * pm + 16 * m + fr) * 136 + 32 * kk + 8 * fq);
; #pragma unroll
;             for (int n = 0; n < 4; ++n) { const int cr = 64 * cn + 16 * n + fr; bn[n] = *(const LAS bf16x8*)(vT + cr * 136 + ((32 * kk + 8 * fq) ^ (((cr >> 3) & 15) << 3))); }
; #pragma unroll
;             for (int m = 0; m < 4; ++m)
; #pragma unroll
;                 for (int n = 0; n < 4; ++n) acc[m][n] = __builtin_amdgcn_mfma_f32_16x16x32_bf16(bn[n], am[m], acc[m][n], 0, 0, 0); }
; #pragma unroll
;         for (int m = 0; m < 4; ++m) { const int p = 64 * pm + 16 * m + fr, row = r0 + p; const float bias = a.in[I_SBS][g * 128 + p];
; #pragma unroll
;             for (int n = 0; n < 4; ++n) { const int c = g * 256 + 64 * cn + 16 * n + 4 * fq;
;                 const u32x2 uu = *(const GAS u32x2*)(Z + (size_t)row * 3072 + 1024 + c);
;                 const float s0 = bflo(uu.x) * (acc[m][n][0] + bias), s1 = bfhi(uu.x) * (acc[m][n][1] + bias), s2 = bflo(uu.y) * (acc[m][n][2] + bias), s3 = bfhi(uu.y) * (acc[m][n][3] + bias);
;                 *(GAS unsigned*)((unsigned char*)MIX + (size_t)row * D + 1024 + c) = pk4_fp8(s0, s1, s2, s3); } }
	v_lshlrev_b32_e32 v118, 16, v194
	s_nop 5
	v_add_f32_e32 v114, v114, v131
	v_add_f32_e32 v115, v115, v131
	v_and_b32_e32 v119, 0xffff0000, v194
	v_mul_f32_e32 v114, v114, v118
	v_mul_f32_e32 v115, v115, v119
	v_med3_f32 v114, v114, s19, v193
	v_med3_f32 v115, v115, s19, v193
	v_cvt_pk_fp8_f32 v127, v114, v115
	v_add_f32_e32 v116, v116, v131
	v_add_f32_e32 v117, v117, v131
	v_lshlrev_b32_e32 v120, 16, v195
	v_and_b32_e32 v121, 0xffff0000, v195
	v_mul_f32_e32 v116, v116, v120
	v_mul_f32_e32 v114, v117, v121
	v_med3_f32 v115, v116, s19, v193
	v_med3_f32 v114, v114, s19, v193
	v_cvt_pk_fp8_f32 v127, v115, v114 op_sel:[0,0,1]
	v_lshl_add_u64 v[118:119], v[80:81], 0, s[10:11]
	v_lshl_add_u64 v[80:81], v[118:119], 0, v[144:145]
	v_mfma_f32_16x16x32_bf16 v[114:117], v[10:13], v[106:109], v[152:155]
	global_store_dword v[80:81], v127, off
	global_load_dwordx2 v[80:81], v[150:151], off offset:2080
	v_mov_b32_e32 v120, v125
	v_mfma_f32_16x16x32_bf16 v[114:117], v[6:9], v[110:113], v[114:117]
	s_waitcnt vmcnt(0)
	v_lshlrev_b32_e32 v121, 16, v80
	s_nop 5
	v_add_f32_e32 v114, v114, v131
	v_add_f32_e32 v115, v115, v131
	v_and_b32_e32 v80, 0xffff0000, v80
	v_mul_f32_e32 v114, v114, v121
	v_mul_f32_e32 v80, v115, v80
	v_med3_f32 v114, v114, s19, v193
	v_med3_f32 v80, v80, s19, v193
	v_cvt_pk_fp8_f32 v120, v114, v80
	v_add_f32_e32 v116, v116, v131
	v_add_f32_e32 v117, v117, v131
	v_lshlrev_b32_e32 v127, 16, v81
	v_and_b32_e32 v81, 0xffff0000, v81
	v_mul_f32_e32 v115, v116, v127
	v_mul_f32_e32 v80, v117, v81
	v_med3_f32 v81, v115, s19, v193
	v_med3_f32 v80, v80, s19, v193
	v_cvt_pk_fp8_f32 v120, v81, v80 op_sel:[0,0,1]
	v_lshl_add_u64 v[114:115], v[118:119], 0, v[104:105]
	v_mfma_f32_16x16x32_bf16 v[80:83], v[98:101], v[106:109], v[82:85]
	global_store_dword v[114:115], v120, off
	v_mov_b32_e32 v114, v125
	s_nop 0
	global_load_dwordx2 v[84:85], v[150:151], off offset:2112
	v_mfma_f32_16x16x32_bf16 v[80:83], v[94:97], v[110:113], v[80:83]
	s_waitcnt vmcnt(0)
	v_lshlrev_b32_e32 v115, 16, v84
	s_nop 5
	v_add_f32_e32 v80, v80, v131
	v_add_f32_e32 v81, v81, v131
	v_and_b32_e32 v84, 0xffff0000, v84
	v_mul_f32_e32 v80, v80, v115
	v_mul_f32_e32 v81, v81, v84
	v_med3_f32 v80, v80, s19, v193
	v_med3_f32 v81, v81, s19, v193
	v_cvt_pk_fp8_f32 v114, v80, v81
	v_add_f32_e32 v82, v82, v131
	v_add_f32_e32 v83, v83, v131
	v_lshlrev_b32_e32 v116, 16, v85
	v_and_b32_e32 v85, 0xffff0000, v85
	v_mul_f32_e32 v82, v82, v116
	v_mul_f32_e32 v80, v83, v85
	v_med3_f32 v81, v82, s19, v193
	v_med3_f32 v80, v80, s19, v193
	v_cvt_pk_fp8_f32 v114, v81, v80 op_sel:[0,0,1]
	v_lshl_add_u64 v[80:81], v[118:119], 0, v[102:103]
	v_mfma_f32_16x16x32_bf16 v[76:79], v[90:93], v[106:109], v[76:79]
	v_mov_b32_e32 v83, v125
	global_store_dword v[80:81], v114, off
	global_load_dwordx2 v[80:81], v[150:151], off offset:2144
	v_mfma_f32_16x16x32_bf16 v[76:79], v[86:89], v[110:113], v[76:79]
	v_or_b32_e32 v82, s2, v171
	v_mad_i64_i32 v[84:85], s[0:1], v82, s17, v[148:149]
	v_mfma_f32_16x16x32_bf16 v[58:61], v[38:41], v[30:33], v[58:61]
	s_waitcnt vmcnt(0)
	v_lshlrev_b32_e32 v106, 16, v80
	s_nop 2
	v_add_f32_e32 v76, v76, v131
	v_add_f32_e32 v77, v77, v131
	v_and_b32_e32 v80, 0xffff0000, v80
	v_mul_f32_e32 v76, v76, v106
	v_mul_f32_e32 v77, v77, v80
	v_med3_f32 v76, v76, s19, v193
	v_med3_f32 v77, v77, s19, v193
	v_cvt_pk_fp8_f32 v83, v76, v77
	v_add_f32_e32 v78, v78, v131
	v_add_f32_e32 v79, v79, v131
	v_lshlrev_b32_e32 v107, 16, v81
	v_and_b32_e32 v81, 0xffff0000, v81
	v_mul_f32_e32 v78, v78, v107
	v_mul_f32_e32 v76, v79, v81
	v_med3_f32 v77, v78, s19, v193
	v_med3_f32 v76, v76, s19, v193
	v_cvt_pk_fp8_f32 v83, v77, v76 op_sel:[0,0,1]
	v_lshl_add_u64 v[78:79], v[118:119], 0, v[74:75]
	v_lshl_add_u64 v[76:77], v[84:85], 0, v[146:147]
	v_mfma_f32_16x16x32_bf16 v[30:33], v[34:37], v[30:33], v[50:53]
	global_store_dword v[78:79], v83, off
	global_load_dwordx2 v[78:79], v[76:77], off offset:2048
	v_ashrrev_i32_e32 v83, 31, v82
	v_mfma_f32_16x16x32_bf16 v[50:53], v[70:73], v[2:5], v[54:57]
	s_nop 2
	ds_read_b128 v[54:57], v191 offset:8832
	ds_read_b128 v[70:73], v191 offset:8896
	v_lshlrev_b64 v[80:81], 11, v[82:83]
	v_mov_b32_e32 v84, v125
	s_waitcnt lgkmcnt(1)
	v_mfma_f32_16x16x32_bf16 v[66:69], v[14:17], v[54:57], v[66:69]
	v_lshl_add_u64 v[80:81], s[92:93], 0, v[80:81]
	s_waitcnt vmcnt(0)
	v_lshlrev_b32_e32 v82, 16, v78
	s_waitcnt lgkmcnt(0)
	v_mfma_f32_16x16x32_bf16 v[66:69], v[18:21], v[70:73], v[66:69]
	v_and_b32_e32 v78, 0xffff0000, v78
	v_lshlrev_b32_e32 v83, 16, v79
	v_and_b32_e32 v79, 0xffff0000, v79
	v_mfma_f32_16x16x32_bf16 v[62:65], v[10:13], v[54:57], v[62:65]
	v_mfma_f32_16x16x32_bf16 v[62:65], v[6:9], v[70:73], v[62:65]
	s_nop 2
	v_add_f32_e32 v66, v66, v133
	v_add_f32_e32 v67, v67, v133
	v_mul_f32_e32 v66, v66, v82
	v_mul_f32_e32 v67, v67, v78
	v_med3_f32 v66, v66, s19, v193
	v_med3_f32 v67, v67, s19, v193
	v_cvt_pk_fp8_f32 v84, v66, v67
	v_add_f32_e32 v68, v68, v133
	v_add_f32_e32 v69, v69, v133
	v_mul_f32_e32 v68, v68, v83
	v_mul_f32_e32 v66, v69, v79
	v_med3_f32 v67, v68, s19, v193
	v_med3_f32 v66, v66, s19, v193
	v_cvt_pk_fp8_f32 v84, v67, v66 op_sel:[0,0,1]
	v_lshl_add_u64 v[66:67], v[80:81], 0, s[10:11]
	v_lshl_add_u64 v[68:69], v[66:67], 0, v[144:145]
	v_add_f32_e32 v62, v62, v133
	global_store_dword v[68:69], v84, off
	global_load_dwordx2 v[68:69], v[76:77], off offset:2080
	v_add_f32_e32 v63, v63, v133
	v_mov_b32_e32 v78, v125
	v_add_f32_e32 v64, v64, v133
	v_add_f32_e32 v65, v65, v133
	v_mfma_f32_16x16x32_bf16 v[58:61], v[98:101], v[54:57], v[58:61]
	s_waitcnt vmcnt(0)
; #define GAS __attribute__((address_space(1)))
; #define LAS __attribute__((address_space(3)))
; __device__ __forceinline__ unsigned pk4_fp8(float a, float b, float c, float d) { int w = 0; w = __builtin_amdgcn_cvt_pk_fp8_f32(sat8(a), sat8(b), w, false); w = __builtin_amdgcn_cvt_pk_fp8_f32(sat8(c), sat8(d), w, true); return (unsigned)w; }
; __device__ __forceinline__ void phase_sgu(const Frame& F, const Args& a) {
;     ...
;         for (int kk = 0; kk < 4; ++kk) { bf16x8 am[4], bn[4];
; #pragma unroll
;             for (int m = 0; m < 4; ++m) am[m] = *(const LAS bf16x8*)(wA + (64 * pm + 16 * m + fr) * 136 + 32 * kk + 8 * fq);
; #pragma unroll
;             for (int n = 0; n < 4; ++n) { const int cr = 64 * cn + 16 * n + fr; bn[n] = *(const LAS bf16x8*)(vT + cr * 136 + ((32 * kk + 8 * fq) ^ (((cr >> 3) & 15) << 3))); }
; #pragma unroll
;             for (int m = 0; m < 4; ++m)
; #pragma unroll
;                 for (int n = 0; n < 4; ++n) acc[m][n] = __builtin_amdgcn_mfma_f32_16x16x32_bf16(bn[n], am[m], acc[m][n], 0, 0, 0); }
; #pragma unroll
;         for (int m = 0; m < 4; ++m) { const int p = 64 * pm + 16 * m + fr, row = r0 + p; const float bias = a.in[I_SBS][g * 128 + p];
; #pragma unroll
;             for (int n = 0; n < 4; ++n) { const int c = g * 256 + 64 * cn + 16 * n + 4 * fq;
;                 const u32x2 uu = *(const GAS u32x2*)(Z + (size_t)row * 3072 + 1024 + c);
;                 const float s0 = bflo(uu.x) * (acc[m][n][0] + bias), s1 = bfhi(uu.x) * (acc[m][n][1] + bias), s2 = bflo(uu.y) * (acc[m][n][2] + bias), s3 = bfhi(uu.y) * (acc[m][n][3] + bias);
;                 *(GAS unsigned*)((unsigned char*)MIX + (size_t)row * D + 1024 + c) = pk4_fp8(s0, s1, s2, s3); } }
;         __syncthreads();
	v_lshlrev_b32_e32 v79, 16, v68
	v_and_b32_e32 v68, 0xffff0000, v68
	v_mul_f32_e32 v62, v62, v79
	v_mul_f32_e32 v63, v63, v68
	v_med3_f32 v62, v62, s19, v193
	v_med3_f32 v63, v63, s19, v193
	v_cvt_pk_fp8_f32 v78, v62, v63
	v_lshlrev_b32_e32 v80, 16, v69
	v_and_b32_e32 v69, 0xffff0000, v69
	v_mul_f32_e32 v64, v64, v80
	v_mul_f32_e32 v62, v65, v69
	v_med3_f32 v63, v64, s19, v193
	v_med3_f32 v62, v62, s19, v193
	v_cvt_pk_fp8_f32 v78, v63, v62 op_sel:[0,0,1]
	v_lshl_add_u64 v[62:63], v[66:67], 0, v[104:105]
	v_mfma_f32_16x16x32_bf16 v[58:61], v[94:97], v[70:73], v[58:61]
	v_mov_b32_e32 v64, v125
	global_store_dword v[62:63], v78, off
	global_load_dwordx2 v[62:63], v[76:77], off offset:2112
	v_mfma_f32_16x16x32_bf16 v[42:45], v[46:49], v[2:5], v[42:45]
	v_mov_b32_e32 v49, v125
	s_nop 2
	v_add_f32_e32 v58, v58, v133
	v_add_f32_e32 v59, v59, v133
	v_add_f32_e32 v60, v60, v133
	v_add_f32_e32 v61, v61, v133
	v_mfma_f32_16x16x32_bf16 v[30:33], v[90:93], v[54:57], v[30:33]
	v_or_b32_e32 v48, s2, v172
	v_mad_i64_i32 v[54:55], s[0:1], v48, s17, v[148:149]
	v_mfma_f32_16x16x32_bf16 v[30:33], v[86:89], v[70:73], v[30:33]
	s_mov_b64 s[0:1], 0
	s_waitcnt vmcnt(0)
	v_lshlrev_b32_e32 v65, 16, v62
	v_and_b32_e32 v62, 0xffff0000, v62
	v_mul_f32_e32 v58, v58, v65
	v_mul_f32_e32 v59, v59, v62
	v_med3_f32 v58, v58, s19, v193
	v_med3_f32 v59, v59, s19, v193
	v_cvt_pk_fp8_f32 v64, v58, v59
	v_lshlrev_b32_e32 v68, 16, v63
	v_and_b32_e32 v63, 0xffff0000, v63
	v_mul_f32_e32 v60, v60, v68
	v_mul_f32_e32 v58, v61, v63
	v_med3_f32 v59, v60, s19, v193
	v_med3_f32 v58, v58, s19, v193
	v_cvt_pk_fp8_f32 v64, v59, v58 op_sel:[0,0,1]
	v_lshl_add_u64 v[58:59], v[66:67], 0, v[102:103]
	v_add_f32_e32 v30, v30, v133
	v_add_f32_e32 v31, v31, v133
	global_store_dword v[58:59], v64, off
	global_load_dwordx2 v[46:47], v[76:77], off offset:2144
	v_add_f32_e32 v32, v32, v133
	v_add_f32_e32 v33, v33, v133
	v_mfma_f32_16x16x32_bf16 v[22:25], v[38:41], v[2:5], v[22:25]
	s_waitcnt vmcnt(0)
	v_lshlrev_b32_e32 v56, 16, v46
	v_and_b32_e32 v46, 0xffff0000, v46
	v_mul_f32_e32 v30, v30, v56
	v_mul_f32_e32 v31, v31, v46
	v_med3_f32 v30, v30, s19, v193
	v_med3_f32 v31, v31, s19, v193
	v_cvt_pk_fp8_f32 v49, v30, v31
	v_lshlrev_b32_e32 v57, 16, v47
	v_and_b32_e32 v47, 0xffff0000, v47
	v_mul_f32_e32 v32, v32, v57
	v_mul_f32_e32 v30, v33, v47
	v_med3_f32 v31, v32, s19, v193
	v_med3_f32 v30, v30, s19, v193
	v_cvt_pk_fp8_f32 v49, v31, v30 op_sel:[0,0,1]
	v_lshl_add_u64 v[30:31], v[66:67], 0, v[74:75]
	v_lshl_add_u64 v[46:47], v[54:55], 0, v[146:147]
	v_mfma_f32_16x16x32_bf16 v[2:5], v[34:37], v[2:5], v[26:29]
	global_store_dword v[30:31], v49, off
	global_load_dwordx2 v[38:39], v[46:47], off offset:2048
	s_nop 0
	ds_read_b128 v[26:29], v191 offset:13184
	ds_read_b128 v[30:33], v191 offset:13248
	s_waitcnt lgkmcnt(1)
	v_mfma_f32_16x16x32_bf16 v[14:17], v[14:17], v[26:29], v[50:53]
	v_mov_b32_e32 v36, v125
	v_ashrrev_i32_e32 v49, 31, v48
	v_lshlrev_b64 v[34:35], 11, v[48:49]
	s_waitcnt lgkmcnt(0)
	v_mfma_f32_16x16x32_bf16 v[14:17], v[18:21], v[30:33], v[14:17]
	v_lshl_add_u64 v[34:35], s[92:93], 0, v[34:35]
	s_waitcnt vmcnt(0)
	v_lshlrev_b32_e32 v18, 16, v38
	s_nop 4
	v_add_f32_e32 v14, v14, v124
	v_add_f32_e32 v15, v15, v124
	v_and_b32_e32 v19, 0xffff0000, v38
	v_mul_f32_e32 v14, v14, v18
	v_mul_f32_e32 v15, v15, v19
	v_med3_f32 v14, v14, s19, v193
	v_med3_f32 v15, v15, s19, v193
	v_cvt_pk_fp8_f32 v36, v14, v15
	v_add_f32_e32 v16, v16, v124
	v_add_f32_e32 v17, v17, v124
	v_lshlrev_b32_e32 v20, 16, v39
	v_and_b32_e32 v21, 0xffff0000, v39
	v_mul_f32_e32 v16, v16, v20
	v_mul_f32_e32 v14, v17, v21
	v_med3_f32 v15, v16, s19, v193
	v_med3_f32 v14, v14, s19, v193
	v_cvt_pk_fp8_f32 v36, v15, v14 op_sel:[0,0,1]
	v_lshl_add_u64 v[14:15], v[34:35], 0, s[10:11]
	v_lshl_add_u64 v[16:17], v[14:15], 0, v[144:145]
	v_mfma_f32_16x16x32_bf16 v[10:13], v[10:13], v[26:29], v[42:45]
	global_store_dword v[16:17], v36, off
	global_load_dwordx2 v[16:17], v[46:47], off offset:2080
	v_mov_b32_e32 v18, v125
	v_mfma_f32_16x16x32_bf16 v[6:9], v[6:9], v[30:33], v[10:13]
	v_mfma_f32_16x16x32_bf16 v[2:5], v[90:93], v[26:29], v[2:5]
	s_waitcnt vmcnt(0)
	s_nop 1
	v_lshlrev_b32_e32 v10, 16, v16
	s_nop 2
	v_add_f32_e32 v6, v6, v124
	v_add_f32_e32 v7, v7, v124
	v_and_b32_e32 v11, 0xffff0000, v16
	v_mul_f32_e32 v6, v6, v10
	v_mul_f32_e32 v7, v7, v11
	v_med3_f32 v6, v6, s19, v193
	v_med3_f32 v7, v7, s19, v193
	v_cvt_pk_fp8_f32 v18, v6, v7
	v_add_f32_e32 v8, v8, v124
	v_add_f32_e32 v9, v9, v124
	v_lshlrev_b32_e32 v12, 16, v17
	v_and_b32_e32 v13, 0xffff0000, v17
	v_mul_f32_e32 v8, v8, v12
	v_mul_f32_e32 v6, v9, v13
	v_med3_f32 v7, v8, s19, v193
	v_med3_f32 v6, v6, s19, v193
	v_cvt_pk_fp8_f32 v18, v7, v6 op_sel:[0,0,1]
	v_lshl_add_u64 v[10:11], v[14:15], 0, v[104:105]
	v_mfma_f32_16x16x32_bf16 v[6:9], v[98:101], v[26:29], v[22:25]
	v_mov_b32_e32 v12, v125
	global_store_dword v[10:11], v18, off
	global_load_dwordx2 v[10:11], v[46:47], off offset:2112
	v_mfma_f32_16x16x32_bf16 v[6:9], v[94:97], v[30:33], v[6:9]
	s_waitcnt vmcnt(0)
	v_lshlrev_b32_e32 v13, 16, v10
	s_nop 5
	v_add_f32_e32 v6, v6, v124
	v_add_f32_e32 v7, v7, v124
	v_and_b32_e32 v10, 0xffff0000, v10
	v_mul_f32_e32 v6, v6, v13
	v_mul_f32_e32 v7, v7, v10
	v_med3_f32 v6, v6, s19, v193
	v_med3_f32 v7, v7, s19, v193
	v_cvt_pk_fp8_f32 v12, v6, v7
	v_add_f32_e32 v8, v8, v124
	v_add_f32_e32 v9, v9, v124
	v_lshlrev_b32_e32 v16, 16, v11
	v_and_b32_e32 v11, 0xffff0000, v11
	v_mul_f32_e32 v8, v8, v16
	v_mul_f32_e32 v6, v9, v11
	v_med3_f32 v7, v8, s19, v193
	v_med3_f32 v6, v6, s19, v193
	v_cvt_pk_fp8_f32 v12, v7, v6 op_sel:[0,0,1]
	v_lshl_add_u64 v[6:7], v[14:15], 0, v[102:103]
	v_mfma_f32_16x16x32_bf16 v[2:5], v[86:89], v[30:33], v[2:5]
	v_mov_b32_e32 v8, v125
	global_store_dword v[6:7], v12, off
	global_load_dwordx2 v[6:7], v[46:47], off offset:2144
	s_waitcnt vmcnt(0)
	v_lshlrev_b32_e32 v9, 16, v6
	s_nop 2
	v_add_f32_e32 v2, v2, v124
	v_add_f32_e32 v3, v3, v124
	v_and_b32_e32 v6, 0xffff0000, v6
	v_mul_f32_e32 v2, v2, v9
	v_mul_f32_e32 v3, v3, v6
	v_med3_f32 v2, v2, s19, v193
	v_med3_f32 v3, v3, s19, v193
	v_cvt_pk_fp8_f32 v8, v2, v3
	v_add_f32_e32 v4, v4, v124
	v_add_f32_e32 v5, v5, v124
	v_lshlrev_b32_e32 v10, 16, v7
	v_and_b32_e32 v7, 0xffff0000, v7
	v_mul_f32_e32 v4, v4, v10
	v_mul_f32_e32 v2, v5, v7
	v_med3_f32 v3, v4, s19, v193
	v_med3_f32 v2, v2, s19, v193
	v_cvt_pk_fp8_f32 v8, v3, v2 op_sel:[0,0,1]
	v_lshl_add_u64 v[2:3], v[14:15], 0, v[74:75]
	global_store_dword v[2:3], v8, off
	s_barrier
	s_branch .LBB0_578
